# MoE gate/up GEMM: the four per-unit gather-offset loads for the next unit issued together with one wait (were four serial load+wait round trips per unit); on top of the five-GEMM phase-start de-serial
# baseline (speedup 1.0000x reference)
; #define PROB_WS() unsigned char* w_ = ws; asm volatile("" : "+s"(w_))
;     __device__ __forceinline__ void a_offs(const Unit& u, unsigned (&off)[2][2], const int (&sR)[2], const int (&sC)[2]) const { const int e = u.e, lt = u.lt; const int cnt = mt.p[32 + e];
;         PROB_WS(); const int* rowtok = (const int*)(w_ + WS_ROWTOK);
; #pragma unroll
;         for (int h = 0; h < 2; ++h)
; #pragma unroll
;             for (int i2 = 0; i2 < 2; ++i2) { const int idx = lt * 256 + h * 128 + sR[i2]; const int tok = idx < cnt ? (rowtok[(size_t)e * MT + idx] >> 1) : 0; off[h][i2] = (unsigned)(tok * 512 + sC[i2]) * 2u; } }
.LBB0_1596:
	s_and_b64 vcc, exec, s[38:39]
	v_mov_b32_e32 v190, v168
	v_mov_b32_e32 v189, v170
	v_mov_b32_e32 v191, v172
	v_mov_b32_e32 v192, v174
	s_cbranch_vccnz .LBB0_1606
	s_lshl_b32 s3, s42, 2
	s_add_i32 s3, s3, 0
	s_add_i32 s3, s3, 0x22900
	v_mov_b32_e32 v4, s3
	ds_read_b32 v8, v4
	s_ashr_i32 s43, s42, 31
	s_mov_b64 s[26:27], s[4:5]
	s_lshl_b64 s[34:35], s[42:43], 16
	s_add_u32 s3, s26, s34
	v_lshlrev_b32_e32 v11, 8, v188
	s_addc_u32 s13, s27, s35
	s_add_u32 s50, s3, 0x5f4000
	v_add_u32_e32 v4, v11, v1
	s_addc_u32 s51, s13, 0
	s_waitcnt lgkmcnt(0)
	v_cmp_lt_i32_e32 vcc, v4, v8
	s_waitcnt vmcnt(0)
	v_mov_b32_e32 v14, 0
	v_mov_b32_e32 v15, 0
	v_mov_b32_e32 v16, 0
	v_mov_b32_e32 v17, 0
	v_ashrrev_i32_e32 v5, 31, v4
	s_and_saveexec_b64 s[52:53], vcc
	s_cbranch_execz .Laoffs_u1
	v_lshl_add_u64 v[18:19], v[4:5], 2, s[50:51]
	flat_load_dword v14, v[18:19]
.Laoffs_u1:
	s_or_b64 exec, exec, s[52:53]
	v_add_u32_e32 v6, v11, v180
	v_cmp_lt_i32_e32 vcc, v6, v8
	v_ashrrev_i32_e32 v7, 31, v6
	s_and_saveexec_b64 s[52:53], vcc
	s_cbranch_execz .Laoffs_u2
	v_lshl_add_u64 v[20:21], v[6:7], 2, s[50:51]
	flat_load_dword v15, v[20:21]
.Laoffs_u2:
	s_or_b64 exec, exec, s[52:53]
	v_or_b32_e32 v13, 0x80, v11
	v_add_u32_e32 v11, v13, v1
	v_cmp_lt_i32_e32 vcc, v11, v8
	s_and_saveexec_b64 s[52:53], vcc
	s_cbranch_execz .Laoffs_u3
	v_lshl_add_u64 v[22:23], v[4:5], 2, s[50:51]
	flat_load_dword v16, v[22:23] offset:512
.Laoffs_u3:
	s_or_b64 exec, exec, s[52:53]
	v_add_u32_e32 v4, v13, v180
	v_cmp_lt_i32_e32 vcc, v4, v8
	s_and_saveexec_b64 s[52:53], vcc
	s_cbranch_execz .Laoffs_u4
	v_lshl_add_u64 v[24:25], v[6:7], 2, s[50:51]
	flat_load_dword v17, v[24:25] offset:512
.Laoffs_u4:
	s_or_b64 exec, exec, s[52:53]
	s_waitcnt vmcnt(0) lgkmcnt(0)
	v_lshlrev_b32_e32 v14, 8, v14
	v_lshlrev_b32_e32 v15, 8, v15
	v_lshlrev_b32_e32 v16, 8, v16
	v_lshlrev_b32_e32 v17, 8, v17
	v_and_b32_e32 v10, 0xfffffe00, v14
	v_and_b32_e32 v9, 0xfffffe00, v15
	v_and_b32_e32 v12, 0xfffffe00, v16
	v_and_b32_e32 v11, 0xfffffe00, v17
	v_add_lshl_u32 v189, v12, v182, 1
	v_add_lshl_u32 v191, v9, v181, 1
	v_add_lshl_u32 v192, v10, v182, 1
	v_add_lshl_u32 v190, v11, v181, 1
